# inproj and outproj K-loops: first K-iteration peeled with C=0 MFMAs too, zeroing removed
# speedup vs baseline: 1.0138x; 1.0002x over previous
.LBB0_136:
	s_ashr_i32 s11, s10, 31
	s_lshl_b64 s[12:13], s[10:11], 19
	s_add_u32 s12, s27, s12
	s_addc_u32 s13, s28, s13
	s_and_b64 s[16:17], s[0:1], exec
	s_cselect_b32 s11, s13, s21
	s_cselect_b32 s51, s12, s20
	s_ashr_i32 s9, s8, 31
	s_lshl_b64 s[16:17], s[8:9], 19
	s_add_u32 s16, s29, s16
	s_addc_u32 s17, s30, s17
	s_and_b64 s[22:23], s[0:1], exec
	s_cselect_b32 s9, s17, s19
	s_cselect_b32 s52, s16, s18
	s_add_u32 s53, s18, 0x100
	s_addc_u32 s54, s19, 0
	s_add_u32 s18, s20, 0x40080
	s_addc_u32 s19, s21, 0
	s_mov_b32 s55, -2
	s_waitcnt vmcnt(0)
	s_add_u32 s20, s18, 0xfffc0080
	s_addc_u32 s21, s19, -1
	s_add_i32 s33, 0, 0x10000
	s_cmp_eq_u32 s55, 12
	s_cselect_b32 s23, s11, s21
	s_cselect_b32 s22, s51, s20
	s_cselect_b32 s21, s9, s54
	s_cselect_b32 s20, s52, s53
	s_add_i32 s44, 0, 0x14000
	v_add_u32_e32 v158, s33, v163
	v_add_u32_e32 v178, s44, v163
	ds_read_b128 v[146:149], v158
	ds_read_b128 v[150:153], v158 offset:1024
	ds_read_b128 v[154:157], v158 offset:2048
	ds_read_b128 v[158:161], v158 offset:3072
	ds_read_b128 v[166:169], v178
	ds_read_b128 v[170:173], v178 offset:1024
	ds_read_b128 v[174:177], v178 offset:2048
	ds_read_b128 v[178:181], v178 offset:3072
	v_lshl_add_u64 v[182:183], s[18:19], 0, v[144:145]
	s_add_i32 m0, s15, 0xc000
	ds_read_b128 v[186:189], v165
	ds_read_b128 v[190:193], v165 offset:1024
	ds_read_b128 v[194:197], v165 offset:2048
	ds_read_b128 v[198:201], v165 offset:3072
	ds_read_b128 v[224:227], v165 offset:4096
	ds_read_b128 v[228:231], v165 offset:5120
	ds_read_b128 v[232:235], v165 offset:6144
	ds_read_b128 v[236:239], v165 offset:7168
	global_load_lds_dwordx4 v[182:183], off
	v_lshl_add_u64 v[182:183], s[18:19], 0, v[142:143]
	s_add_i32 m0, s15, 0xe000
	s_nop 0
	global_load_lds_dwordx4 v[182:183], off
	s_waitcnt vmcnt(8)
	s_waitcnt lgkmcnt(0)
	s_barrier
	s_setprio 1
	s_waitcnt lgkmcnt(0)
	v_mfma_f32_16x16x32_bf16 v[130:133], v[146:149], v[186:189], 0
	v_mfma_f32_16x16x32_bf16 v[126:129], v[154:157], v[186:189], 0
	v_mfma_f32_16x16x32_bf16 v[122:125], v[146:149], v[194:197], 0
	v_mfma_f32_16x16x32_bf16 v[118:121], v[154:157], v[194:197], 0
	v_mfma_f32_16x16x32_bf16 v[114:117], v[146:149], v[224:227], 0
	v_mfma_f32_16x16x32_bf16 v[110:113], v[154:157], v[224:227], 0
	v_mfma_f32_16x16x32_bf16 v[98:101], v[146:149], v[232:235], 0
	v_mfma_f32_16x16x32_bf16 v[94:97], v[154:157], v[232:235], 0
	v_mfma_f32_16x16x32_bf16 v[130:133], v[150:153], v[190:193], v[130:133]
	v_mfma_f32_16x16x32_bf16 v[126:129], v[158:161], v[190:193], v[126:129]
	v_mfma_f32_16x16x32_bf16 v[122:125], v[150:153], v[198:201], v[122:125]
	v_mfma_f32_16x16x32_bf16 v[118:121], v[158:161], v[198:201], v[118:121]
	v_mfma_f32_16x16x32_bf16 v[114:117], v[150:153], v[228:231], v[114:117]
	v_mfma_f32_16x16x32_bf16 v[110:113], v[158:161], v[228:231], v[110:113]
	v_mfma_f32_16x16x32_bf16 v[98:101], v[150:153], v[236:239], v[98:101]
	v_mfma_f32_16x16x32_bf16 v[94:97], v[158:161], v[236:239], v[94:97]
	s_setprio 0
	s_setprio 1
	v_mfma_f32_16x16x32_bf16 v[106:109], v[166:169], v[186:189], 0
	v_mfma_f32_16x16x32_bf16 v[102:105], v[174:177], v[186:189], 0
	v_mfma_f32_16x16x32_bf16 v[90:93], v[166:169], v[194:197], 0
	v_mfma_f32_16x16x32_bf16 v[86:89], v[174:177], v[194:197], 0
	v_mfma_f32_16x16x32_bf16 v[82:85], v[166:169], v[224:227], 0
	v_mfma_f32_16x16x32_bf16 v[78:81], v[174:177], v[224:227], 0
	v_mfma_f32_16x16x32_bf16 v[74:77], v[166:169], v[232:235], 0
	v_mfma_f32_16x16x32_bf16 v[70:73], v[174:177], v[232:235], 0
	v_mfma_f32_16x16x32_bf16 v[106:109], v[170:173], v[190:193], v[106:109]
	v_mfma_f32_16x16x32_bf16 v[102:105], v[178:181], v[190:193], v[102:105]
	v_mfma_f32_16x16x32_bf16 v[90:93], v[170:173], v[198:201], v[90:93]
	v_mfma_f32_16x16x32_bf16 v[86:89], v[178:181], v[198:201], v[86:89]
	v_mfma_f32_16x16x32_bf16 v[82:85], v[170:173], v[228:231], v[82:85]
	v_mfma_f32_16x16x32_bf16 v[78:81], v[178:181], v[228:231], v[78:81]
	v_mfma_f32_16x16x32_bf16 v[74:77], v[170:173], v[236:239], v[74:77]
	v_mfma_f32_16x16x32_bf16 v[70:73], v[178:181], v[236:239], v[70:73]
	s_setprio 0
	s_barrier
	s_add_i32 s33, s33, s31
	v_lshl_add_u64 v[182:183], s[20:21], 0, v[0:1]
	s_mov_b32 m0, s33
	ds_read_b128 v[186:189], v165 offset:16384
	ds_read_b128 v[190:193], v165 offset:17408
	ds_read_b128 v[194:197], v165 offset:18432
	ds_read_b128 v[198:201], v165 offset:19456
	ds_read_b128 v[224:227], v165 offset:20480
	ds_read_b128 v[228:231], v165 offset:21504
	ds_read_b128 v[232:235], v165 offset:22528
	ds_read_b128 v[236:239], v165 offset:23552
	global_load_lds_dwordx4 v[182:183], off
	s_add_i32 m0, s33, 0x2000
	s_add_u32 s40, s20, 0x40000
	v_lshl_add_u64 v[184:185], s[20:21], 0, v[134:135]
	s_addc_u32 s41, s21, 0
	s_add_i32 s33, s44, s31
	global_load_lds_dwordx4 v[184:185], off
	v_lshl_add_u64 v[202:203], s[40:41], 0, v[0:1]
	s_mov_b32 m0, s33
	v_lshl_add_u64 v[210:211], s[22:23], 0, v[136:137]
	global_load_lds_dwordx4 v[202:203], off
	v_lshl_add_u64 v[202:203], s[40:41], 0, v[134:135]
	s_add_i32 m0, s33, 0x2000
	s_nop 0
	global_load_lds_dwordx4 v[202:203], off
	v_lshl_add_u64 v[202:203], s[22:23], 0, v[138:139]
	s_mov_b32 m0, s15
	s_nop 0
	global_load_lds_dwordx4 v[202:203], off
	s_mov_b32 m0, s35
	s_nop 0
	global_load_lds_dwordx4 v[210:211], off
	s_waitcnt vmcnt(8)
	s_waitcnt lgkmcnt(0)
	s_barrier
	s_setprio 1
	s_waitcnt lgkmcnt(0)
	v_mfma_f32_16x16x32_bf16 v[66:69], v[146:149], v[186:189], 0
	v_mfma_f32_16x16x32_bf16 v[62:65], v[154:157], v[186:189], 0
	v_mfma_f32_16x16x32_bf16 v[58:61], v[146:149], v[194:197], 0
	v_mfma_f32_16x16x32_bf16 v[54:57], v[154:157], v[194:197], 0
	v_mfma_f32_16x16x32_bf16 v[50:53], v[146:149], v[224:227], 0
	v_mfma_f32_16x16x32_bf16 v[46:49], v[154:157], v[224:227], 0
	v_mfma_f32_16x16x32_bf16 v[30:33], v[146:149], v[232:235], 0
	v_mfma_f32_16x16x32_bf16 v[26:29], v[154:157], v[232:235], 0
	v_mfma_f32_16x16x32_bf16 v[66:69], v[150:153], v[190:193], v[66:69]
	v_mfma_f32_16x16x32_bf16 v[62:65], v[158:161], v[190:193], v[62:65]
	v_mfma_f32_16x16x32_bf16 v[58:61], v[150:153], v[198:201], v[58:61]
	v_mfma_f32_16x16x32_bf16 v[54:57], v[158:161], v[198:201], v[54:57]
	v_mfma_f32_16x16x32_bf16 v[50:53], v[150:153], v[228:231], v[50:53]
	v_mfma_f32_16x16x32_bf16 v[46:49], v[158:161], v[228:231], v[46:49]
	v_mfma_f32_16x16x32_bf16 v[30:33], v[150:153], v[236:239], v[30:33]
	v_mfma_f32_16x16x32_bf16 v[26:29], v[158:161], v[236:239], v[26:29]
	s_setprio 0
	s_setprio 1
	v_mfma_f32_16x16x32_bf16 v[42:45], v[166:169], v[186:189], 0
	v_mfma_f32_16x16x32_bf16 v[38:41], v[174:177], v[186:189], 0
	v_mfma_f32_16x16x32_bf16 v[22:25], v[166:169], v[194:197], 0
	v_mfma_f32_16x16x32_bf16 v[18:21], v[174:177], v[194:197], 0
	v_mfma_f32_16x16x32_bf16 v[14:17], v[166:169], v[224:227], 0
	v_mfma_f32_16x16x32_bf16 v[10:13], v[174:177], v[224:227], 0
	v_mfma_f32_16x16x32_bf16 v[6:9], v[166:169], v[232:235], 0
	v_mfma_f32_16x16x32_bf16 v[2:5], v[174:177], v[232:235], 0
	v_mfma_f32_16x16x32_bf16 v[42:45], v[170:173], v[190:193], v[42:45]
	v_mfma_f32_16x16x32_bf16 v[38:41], v[178:181], v[190:193], v[38:41]
	v_mfma_f32_16x16x32_bf16 v[22:25], v[170:173], v[198:201], v[22:25]
	v_mfma_f32_16x16x32_bf16 v[18:21], v[178:181], v[198:201], v[18:21]
	v_mfma_f32_16x16x32_bf16 v[14:17], v[170:173], v[228:231], v[14:17]
	v_mfma_f32_16x16x32_bf16 v[10:13], v[178:181], v[228:231], v[10:13]
	v_mfma_f32_16x16x32_bf16 v[6:9], v[170:173], v[236:239], v[6:9]
	v_mfma_f32_16x16x32_bf16 v[2:5], v[178:181], v[236:239], v[2:5]
	s_setprio 0
	s_barrier
	s_add_i32 s33, 0, 0x18000
	s_add_i32 s40, 0, 0x1c000
	v_add_u32_e32 v158, s33, v163
	v_add_u32_e32 v178, s40, v163
	ds_read_b128 v[146:149], v158
	ds_read_b128 v[150:153], v158 offset:1024
	ds_read_b128 v[154:157], v158 offset:2048
	ds_read_b128 v[158:161], v158 offset:3072
	ds_read_b128 v[166:169], v178
	ds_read_b128 v[170:173], v178 offset:1024
	ds_read_b128 v[174:177], v178 offset:2048
	ds_read_b128 v[178:181], v178 offset:3072
	s_add_u32 s22, s22, 0x40000
	s_addc_u32 s23, s23, 0
	s_mov_b32 m0, s36
	v_lshl_add_u64 v[218:219], s[22:23], 0, v[138:139]
	ds_read_b128 v[186:189], v165 offset:32768
	ds_read_b128 v[190:193], v165 offset:33792
	ds_read_b128 v[194:197], v165 offset:34816
	ds_read_b128 v[198:201], v165 offset:35840
	ds_read_b128 v[224:227], v165 offset:36864
	ds_read_b128 v[228:231], v165 offset:37888
	ds_read_b128 v[232:235], v165 offset:38912
	ds_read_b128 v[236:239], v165 offset:39936
	global_load_lds_dwordx4 v[218:219], off
	v_lshl_add_u64 v[218:219], s[22:23], 0, v[136:137]
	s_mov_b32 m0, s37
	s_nop 0
	global_load_lds_dwordx4 v[218:219], off
	s_waitcnt vmcnt(8)
	s_waitcnt lgkmcnt(0)
	s_barrier
	s_setprio 1
	s_waitcnt lgkmcnt(0)
	v_mfma_f32_16x16x32_bf16 v[130:133], v[146:149], v[186:189], v[130:133]
	v_mfma_f32_16x16x32_bf16 v[126:129], v[154:157], v[186:189], v[126:129]
	v_mfma_f32_16x16x32_bf16 v[122:125], v[146:149], v[194:197], v[122:125]
	v_mfma_f32_16x16x32_bf16 v[118:121], v[154:157], v[194:197], v[118:121]
	v_mfma_f32_16x16x32_bf16 v[114:117], v[146:149], v[224:227], v[114:117]
	v_mfma_f32_16x16x32_bf16 v[110:113], v[154:157], v[224:227], v[110:113]
	v_mfma_f32_16x16x32_bf16 v[98:101], v[146:149], v[232:235], v[98:101]
	v_mfma_f32_16x16x32_bf16 v[94:97], v[154:157], v[232:235], v[94:97]
	v_mfma_f32_16x16x32_bf16 v[130:133], v[150:153], v[190:193], v[130:133]
	v_mfma_f32_16x16x32_bf16 v[126:129], v[158:161], v[190:193], v[126:129]
	v_mfma_f32_16x16x32_bf16 v[122:125], v[150:153], v[198:201], v[122:125]
	v_mfma_f32_16x16x32_bf16 v[118:121], v[158:161], v[198:201], v[118:121]
	v_mfma_f32_16x16x32_bf16 v[114:117], v[150:153], v[228:231], v[114:117]
	v_mfma_f32_16x16x32_bf16 v[110:113], v[158:161], v[228:231], v[110:113]
	v_mfma_f32_16x16x32_bf16 v[98:101], v[150:153], v[236:239], v[98:101]
	v_mfma_f32_16x16x32_bf16 v[94:97], v[158:161], v[236:239], v[94:97]
	s_setprio 0
	s_setprio 1
	v_mfma_f32_16x16x32_bf16 v[106:109], v[166:169], v[186:189], v[106:109]
	v_mfma_f32_16x16x32_bf16 v[102:105], v[174:177], v[186:189], v[102:105]
	v_mfma_f32_16x16x32_bf16 v[90:93], v[166:169], v[194:197], v[90:93]
	v_mfma_f32_16x16x32_bf16 v[86:89], v[174:177], v[194:197], v[86:89]
	v_mfma_f32_16x16x32_bf16 v[82:85], v[166:169], v[224:227], v[82:85]
	v_mfma_f32_16x16x32_bf16 v[78:81], v[174:177], v[224:227], v[78:81]
	v_mfma_f32_16x16x32_bf16 v[74:77], v[166:169], v[232:235], v[74:77]
	v_mfma_f32_16x16x32_bf16 v[70:73], v[174:177], v[232:235], v[70:73]
	v_mfma_f32_16x16x32_bf16 v[106:109], v[170:173], v[190:193], v[106:109]
	v_mfma_f32_16x16x32_bf16 v[102:105], v[178:181], v[190:193], v[102:105]
	v_mfma_f32_16x16x32_bf16 v[90:93], v[170:173], v[198:201], v[90:93]
	v_mfma_f32_16x16x32_bf16 v[86:89], v[178:181], v[198:201], v[86:89]
	v_mfma_f32_16x16x32_bf16 v[82:85], v[170:173], v[228:231], v[82:85]
	v_mfma_f32_16x16x32_bf16 v[78:81], v[178:181], v[228:231], v[78:81]
	v_mfma_f32_16x16x32_bf16 v[74:77], v[170:173], v[236:239], v[74:77]
	v_mfma_f32_16x16x32_bf16 v[70:73], v[178:181], v[236:239], v[70:73]
	s_setprio 0
	s_barrier
	s_add_i32 s22, s33, s31
	v_lshl_add_u64 v[182:183], v[182:183], 0, s[46:47]
	s_mov_b32 m0, s22
	ds_read_b128 v[186:189], v165 offset:49152
	ds_read_b128 v[190:193], v165 offset:50176
	ds_read_b128 v[194:197], v165 offset:51200
	ds_read_b128 v[198:201], v165 offset:52224
	ds_read_b128 v[224:227], v165 offset:53248
	ds_read_b128 v[228:231], v165 offset:54272
	ds_read_b128 v[232:235], v165 offset:55296
	ds_read_b128 v[236:239], v165 offset:56320
	global_load_lds_dwordx4 v[182:183], off
	s_add_i32 m0, s22, 0x2000
	s_add_u32 s20, s20, 0x40080
	v_lshl_add_u64 v[182:183], v[184:185], 0, s[46:47]
	s_addc_u32 s21, s21, 0
	s_add_i32 s22, s40, s31
	global_load_lds_dwordx4 v[182:183], off
	v_lshl_add_u64 v[182:183], s[20:21], 0, v[0:1]
	s_mov_b32 m0, s22
	s_nop 0
	global_load_lds_dwordx4 v[182:183], off
	v_lshl_add_u64 v[182:183], s[20:21], 0, v[134:135]
	s_add_i32 m0, s22, 0x2000
	s_nop 0
	global_load_lds_dwordx4 v[182:183], off
	v_lshl_add_u64 v[182:183], v[202:203], 0, s[46:47]
	s_mov_b32 m0, s38
	s_nop 0
	global_load_lds_dwordx4 v[182:183], off
	v_lshl_add_u64 v[182:183], v[210:211], 0, s[46:47]
	s_mov_b32 m0, s39
	s_nop 0
	global_load_lds_dwordx4 v[182:183], off
	s_waitcnt vmcnt(8)
	s_waitcnt lgkmcnt(0)
	s_barrier
	s_setprio 1
	s_waitcnt lgkmcnt(0)
	v_mfma_f32_16x16x32_bf16 v[66:69], v[146:149], v[186:189], v[66:69]
	v_mfma_f32_16x16x32_bf16 v[62:65], v[154:157], v[186:189], v[62:65]
	v_mfma_f32_16x16x32_bf16 v[58:61], v[146:149], v[194:197], v[58:61]
	v_mfma_f32_16x16x32_bf16 v[54:57], v[154:157], v[194:197], v[54:57]
	v_mfma_f32_16x16x32_bf16 v[50:53], v[146:149], v[224:227], v[50:53]
	v_mfma_f32_16x16x32_bf16 v[46:49], v[154:157], v[224:227], v[46:49]
	v_mfma_f32_16x16x32_bf16 v[30:33], v[146:149], v[232:235], v[30:33]
	v_mfma_f32_16x16x32_bf16 v[26:29], v[154:157], v[232:235], v[26:29]
	v_mfma_f32_16x16x32_bf16 v[66:69], v[150:153], v[190:193], v[66:69]
	v_mfma_f32_16x16x32_bf16 v[62:65], v[158:161], v[190:193], v[62:65]
	v_mfma_f32_16x16x32_bf16 v[58:61], v[150:153], v[198:201], v[58:61]
	v_mfma_f32_16x16x32_bf16 v[54:57], v[158:161], v[198:201], v[54:57]
	v_mfma_f32_16x16x32_bf16 v[50:53], v[150:153], v[228:231], v[50:53]
	v_mfma_f32_16x16x32_bf16 v[46:49], v[158:161], v[228:231], v[46:49]
	v_mfma_f32_16x16x32_bf16 v[30:33], v[150:153], v[236:239], v[30:33]
	v_mfma_f32_16x16x32_bf16 v[26:29], v[158:161], v[236:239], v[26:29]
	s_setprio 0
	s_setprio 1
	v_mfma_f32_16x16x32_bf16 v[42:45], v[166:169], v[186:189], v[42:45]
	v_mfma_f32_16x16x32_bf16 v[38:41], v[174:177], v[186:189], v[38:41]
	v_mfma_f32_16x16x32_bf16 v[22:25], v[166:169], v[194:197], v[22:25]
	v_mfma_f32_16x16x32_bf16 v[18:21], v[174:177], v[194:197], v[18:21]
	v_mfma_f32_16x16x32_bf16 v[14:17], v[166:169], v[224:227], v[14:17]
	v_mfma_f32_16x16x32_bf16 v[10:13], v[174:177], v[224:227], v[10:13]
	v_mfma_f32_16x16x32_bf16 v[6:9], v[166:169], v[232:235], v[6:9]
	v_mfma_f32_16x16x32_bf16 v[2:5], v[174:177], v[232:235], v[2:5]
	v_mfma_f32_16x16x32_bf16 v[42:45], v[170:173], v[190:193], v[42:45]
	v_mfma_f32_16x16x32_bf16 v[38:41], v[178:181], v[190:193], v[38:41]
	v_mfma_f32_16x16x32_bf16 v[22:25], v[170:173], v[198:201], v[22:25]
	v_mfma_f32_16x16x32_bf16 v[18:21], v[178:181], v[198:201], v[18:21]
	v_mfma_f32_16x16x32_bf16 v[14:17], v[170:173], v[228:231], v[14:17]
	v_mfma_f32_16x16x32_bf16 v[10:13], v[178:181], v[228:231], v[10:13]
	v_mfma_f32_16x16x32_bf16 v[6:9], v[170:173], v[236:239], v[6:9]
	v_mfma_f32_16x16x32_bf16 v[2:5], v[178:181], v[236:239], v[2:5]
	s_setprio 0
	s_barrier
	s_add_i32 s55, s55, 2
	s_add_u32 s53, s53, 0x100
	s_addc_u32 s54, s54, 0
	s_add_u32 s18, s18, 0x100
	s_addc_u32 s19, s19, 0

.LBB0_1320:
	s_ashr_i32 s13, s12, 31
	s_lshl_b64 s[14:15], s[12:13], 19
	s_add_u32 s14, s28, s14
	s_addc_u32 s15, s29, s15
	s_and_b64 s[16:17], s[0:1], exec
	s_cselect_b32 s13, s15, s21
	s_cselect_b32 s51, s14, s20
	s_ashr_i32 s11, s10, 31
	s_lshl_b64 s[16:17], s[10:11], 19
	s_add_u32 s16, s30, s16
	s_addc_u32 s17, s31, s17
	s_and_b64 s[22:23], s[0:1], exec
	s_cselect_b32 s11, s17, s19
	s_cselect_b32 s52, s16, s18
	s_add_u32 s53, s18, 0x100
	s_addc_u32 s54, s19, 0
	s_add_u32 s18, s20, 0x40080
	s_addc_u32 s19, s21, 0
	s_mov_b32 s55, -2
	s_add_u32 s20, s18, 0xfffc0080
	s_addc_u32 s21, s19, -1
	s_add_i32 s33, 0, 0x10000
	s_cmp_eq_u32 s55, 12
	s_cselect_b32 s23, s13, s21
	s_cselect_b32 s22, s51, s20
	s_cselect_b32 s21, s11, s54
	s_cselect_b32 s20, s52, s53
	s_add_i32 s44, 0, 0x14000
	v_add_u32_e32 v158, s33, v162
	v_add_u32_e32 v165, s44, v162
	ds_read_b128 v[146:149], v158
	ds_read_b128 v[150:153], v158 offset:1024
	ds_read_b128 v[154:157], v158 offset:2048
	ds_read_b128 v[158:161], v158 offset:3072
	ds_read_b128 v[166:169], v165
	ds_read_b128 v[170:173], v165 offset:1024
	ds_read_b128 v[174:177], v165 offset:2048
	ds_read_b128 v[178:181], v165 offset:3072
	v_lshl_add_u64 v[182:183], s[18:19], 0, v[144:145]
	s_add_i32 m0, s9, 0xc000
	ds_read_b128 v[186:189], v164
	ds_read_b128 v[190:193], v164 offset:1024
	ds_read_b128 v[194:197], v164 offset:2048
	ds_read_b128 v[198:201], v164 offset:3072
	ds_read_b128 v[224:227], v164 offset:4096
	ds_read_b128 v[228:231], v164 offset:5120
	ds_read_b128 v[232:235], v164 offset:6144
	ds_read_b128 v[236:239], v164 offset:7168
	global_load_lds_dwordx4 v[182:183], off
	v_lshl_add_u64 v[182:183], s[18:19], 0, v[142:143]
	s_add_i32 m0, s9, 0xe000
	s_nop 0
	global_load_lds_dwordx4 v[182:183], off
	s_waitcnt vmcnt(8)
	s_waitcnt lgkmcnt(0)
	s_barrier
	s_setprio 1
	s_waitcnt lgkmcnt(0)
	v_mfma_f32_16x16x32_bf16 v[130:133], v[146:149], v[186:189], 0
	v_mfma_f32_16x16x32_bf16 v[126:129], v[154:157], v[186:189], 0
	v_mfma_f32_16x16x32_bf16 v[122:125], v[146:149], v[194:197], 0
	v_mfma_f32_16x16x32_bf16 v[118:121], v[154:157], v[194:197], 0
	v_mfma_f32_16x16x32_bf16 v[114:117], v[146:149], v[224:227], 0
	v_mfma_f32_16x16x32_bf16 v[106:109], v[154:157], v[224:227], 0
	v_mfma_f32_16x16x32_bf16 v[98:101], v[146:149], v[232:235], 0
	v_mfma_f32_16x16x32_bf16 v[90:93], v[154:157], v[232:235], 0
	v_mfma_f32_16x16x32_bf16 v[130:133], v[150:153], v[190:193], v[130:133]
	v_mfma_f32_16x16x32_bf16 v[126:129], v[158:161], v[190:193], v[126:129]
	v_mfma_f32_16x16x32_bf16 v[122:125], v[150:153], v[198:201], v[122:125]
	v_mfma_f32_16x16x32_bf16 v[118:121], v[158:161], v[198:201], v[118:121]
	v_mfma_f32_16x16x32_bf16 v[114:117], v[150:153], v[228:231], v[114:117]
	v_mfma_f32_16x16x32_bf16 v[106:109], v[158:161], v[228:231], v[106:109]
	v_mfma_f32_16x16x32_bf16 v[98:101], v[150:153], v[236:239], v[98:101]
	v_mfma_f32_16x16x32_bf16 v[90:93], v[158:161], v[236:239], v[90:93]
	s_setprio 0
	s_setprio 1
	v_mfma_f32_16x16x32_bf16 v[110:113], v[166:169], v[186:189], 0
	v_mfma_f32_16x16x32_bf16 v[102:105], v[174:177], v[186:189], 0
	v_mfma_f32_16x16x32_bf16 v[94:97], v[166:169], v[194:197], 0
	v_mfma_f32_16x16x32_bf16 v[86:89], v[174:177], v[194:197], 0
	v_mfma_f32_16x16x32_bf16 v[82:85], v[166:169], v[224:227], 0
	v_mfma_f32_16x16x32_bf16 v[78:81], v[174:177], v[224:227], 0
	v_mfma_f32_16x16x32_bf16 v[74:77], v[166:169], v[232:235], 0
	v_mfma_f32_16x16x32_bf16 v[70:73], v[174:177], v[232:235], 0
	v_mfma_f32_16x16x32_bf16 v[110:113], v[170:173], v[190:193], v[110:113]
	v_mfma_f32_16x16x32_bf16 v[102:105], v[178:181], v[190:193], v[102:105]
	v_mfma_f32_16x16x32_bf16 v[94:97], v[170:173], v[198:201], v[94:97]
	v_mfma_f32_16x16x32_bf16 v[86:89], v[178:181], v[198:201], v[86:89]
	v_mfma_f32_16x16x32_bf16 v[82:85], v[170:173], v[228:231], v[82:85]
	v_mfma_f32_16x16x32_bf16 v[78:81], v[178:181], v[228:231], v[78:81]
	v_mfma_f32_16x16x32_bf16 v[74:77], v[170:173], v[236:239], v[74:77]
	v_mfma_f32_16x16x32_bf16 v[70:73], v[178:181], v[236:239], v[70:73]
	s_setprio 0
	s_barrier
	s_add_i32 s33, s33, s34
	v_lshl_add_u64 v[182:183], s[20:21], 0, v[0:1]
	s_mov_b32 m0, s33
	ds_read_b128 v[186:189], v164 offset:16384
	ds_read_b128 v[190:193], v164 offset:17408
	ds_read_b128 v[194:197], v164 offset:18432
	ds_read_b128 v[198:201], v164 offset:19456
	ds_read_b128 v[224:227], v164 offset:20480
	ds_read_b128 v[228:231], v164 offset:21504
	ds_read_b128 v[232:235], v164 offset:22528
	ds_read_b128 v[236:239], v164 offset:23552
	global_load_lds_dwordx4 v[182:183], off
	s_add_i32 m0, s33, 0x2000
	s_add_u32 s40, s20, 0x40000
	v_lshl_add_u64 v[184:185], s[20:21], 0, v[138:139]
	s_addc_u32 s41, s21, 0
	s_add_i32 s33, s44, s34
	global_load_lds_dwordx4 v[184:185], off
	v_lshl_add_u64 v[202:203], s[40:41], 0, v[0:1]
	s_mov_b32 m0, s33
	v_lshl_add_u64 v[210:211], s[22:23], 0, v[136:137]
	global_load_lds_dwordx4 v[202:203], off
	v_lshl_add_u64 v[202:203], s[40:41], 0, v[138:139]
	s_add_i32 m0, s33, 0x2000
	s_nop 0
	global_load_lds_dwordx4 v[202:203], off
	v_lshl_add_u64 v[202:203], s[22:23], 0, v[134:135]
	s_mov_b32 m0, s9
	s_nop 0
	global_load_lds_dwordx4 v[202:203], off
	s_mov_b32 m0, s35
	s_nop 0
	global_load_lds_dwordx4 v[210:211], off
	s_waitcnt vmcnt(8)
	s_waitcnt lgkmcnt(0)
	s_barrier
	s_setprio 1
	s_waitcnt lgkmcnt(0)
	v_mfma_f32_16x16x32_bf16 v[66:69], v[146:149], v[186:189], 0
	v_mfma_f32_16x16x32_bf16 v[62:65], v[154:157], v[186:189], 0
	v_mfma_f32_16x16x32_bf16 v[58:61], v[146:149], v[194:197], 0
	v_mfma_f32_16x16x32_bf16 v[54:57], v[154:157], v[194:197], 0
	v_mfma_f32_16x16x32_bf16 v[50:53], v[146:149], v[224:227], 0
	v_mfma_f32_16x16x32_bf16 v[42:45], v[154:157], v[224:227], 0
	v_mfma_f32_16x16x32_bf16 v[30:33], v[146:149], v[232:235], 0
	v_mfma_f32_16x16x32_bf16 v[22:25], v[154:157], v[232:235], 0
	v_mfma_f32_16x16x32_bf16 v[66:69], v[150:153], v[190:193], v[66:69]
	v_mfma_f32_16x16x32_bf16 v[62:65], v[158:161], v[190:193], v[62:65]
	v_mfma_f32_16x16x32_bf16 v[58:61], v[150:153], v[198:201], v[58:61]
	v_mfma_f32_16x16x32_bf16 v[54:57], v[158:161], v[198:201], v[54:57]
	v_mfma_f32_16x16x32_bf16 v[50:53], v[150:153], v[228:231], v[50:53]
	v_mfma_f32_16x16x32_bf16 v[42:45], v[158:161], v[228:231], v[42:45]
	v_mfma_f32_16x16x32_bf16 v[30:33], v[150:153], v[236:239], v[30:33]
	v_mfma_f32_16x16x32_bf16 v[22:25], v[158:161], v[236:239], v[22:25]
	s_setprio 0
	s_setprio 1
	v_mfma_f32_16x16x32_bf16 v[46:49], v[166:169], v[186:189], 0
	v_mfma_f32_16x16x32_bf16 v[38:41], v[174:177], v[186:189], 0
	v_mfma_f32_16x16x32_bf16 v[26:29], v[166:169], v[194:197], 0
	v_mfma_f32_16x16x32_bf16 v[18:21], v[174:177], v[194:197], 0
	v_mfma_f32_16x16x32_bf16 v[14:17], v[166:169], v[224:227], 0
	v_mfma_f32_16x16x32_bf16 v[10:13], v[174:177], v[224:227], 0
	v_mfma_f32_16x16x32_bf16 v[6:9], v[166:169], v[232:235], 0
	v_mfma_f32_16x16x32_bf16 v[2:5], v[174:177], v[232:235], 0
	v_mfma_f32_16x16x32_bf16 v[46:49], v[170:173], v[190:193], v[46:49]
	v_mfma_f32_16x16x32_bf16 v[38:41], v[178:181], v[190:193], v[38:41]
	v_mfma_f32_16x16x32_bf16 v[26:29], v[170:173], v[198:201], v[26:29]
	v_mfma_f32_16x16x32_bf16 v[18:21], v[178:181], v[198:201], v[18:21]
	v_mfma_f32_16x16x32_bf16 v[14:17], v[170:173], v[228:231], v[14:17]
	v_mfma_f32_16x16x32_bf16 v[10:13], v[178:181], v[228:231], v[10:13]
	v_mfma_f32_16x16x32_bf16 v[6:9], v[170:173], v[236:239], v[6:9]
	v_mfma_f32_16x16x32_bf16 v[2:5], v[178:181], v[236:239], v[2:5]
	s_setprio 0
	s_barrier
	s_add_i32 s33, 0, 0x18000
	s_add_i32 s40, 0, 0x1c000
	v_add_u32_e32 v158, s33, v162
	v_add_u32_e32 v165, s40, v162
	ds_read_b128 v[146:149], v158
	ds_read_b128 v[150:153], v158 offset:1024
	ds_read_b128 v[154:157], v158 offset:2048
	ds_read_b128 v[158:161], v158 offset:3072
	ds_read_b128 v[166:169], v165
	ds_read_b128 v[170:173], v165 offset:1024
	ds_read_b128 v[174:177], v165 offset:2048
	ds_read_b128 v[178:181], v165 offset:3072
	s_add_u32 s22, s22, 0x40000
	s_addc_u32 s23, s23, 0
	s_mov_b32 m0, s36
	v_lshl_add_u64 v[218:219], s[22:23], 0, v[134:135]
	ds_read_b128 v[186:189], v164 offset:32768
	ds_read_b128 v[190:193], v164 offset:33792
	ds_read_b128 v[194:197], v164 offset:34816
	ds_read_b128 v[198:201], v164 offset:35840
	ds_read_b128 v[224:227], v164 offset:36864
	ds_read_b128 v[228:231], v164 offset:37888
	ds_read_b128 v[232:235], v164 offset:38912
	ds_read_b128 v[236:239], v164 offset:39936
	global_load_lds_dwordx4 v[218:219], off
	v_lshl_add_u64 v[218:219], s[22:23], 0, v[136:137]
	s_mov_b32 m0, s37
	s_nop 0
	global_load_lds_dwordx4 v[218:219], off
	s_waitcnt vmcnt(8)
	s_waitcnt lgkmcnt(0)
	s_barrier
	s_setprio 1
	s_waitcnt lgkmcnt(0)
	v_mfma_f32_16x16x32_bf16 v[130:133], v[146:149], v[186:189], v[130:133]
	v_mfma_f32_16x16x32_bf16 v[126:129], v[154:157], v[186:189], v[126:129]
	v_mfma_f32_16x16x32_bf16 v[122:125], v[146:149], v[194:197], v[122:125]
	v_mfma_f32_16x16x32_bf16 v[118:121], v[154:157], v[194:197], v[118:121]
	v_mfma_f32_16x16x32_bf16 v[114:117], v[146:149], v[224:227], v[114:117]
	v_mfma_f32_16x16x32_bf16 v[106:109], v[154:157], v[224:227], v[106:109]
	v_mfma_f32_16x16x32_bf16 v[98:101], v[146:149], v[232:235], v[98:101]
	v_mfma_f32_16x16x32_bf16 v[90:93], v[154:157], v[232:235], v[90:93]
	v_mfma_f32_16x16x32_bf16 v[130:133], v[150:153], v[190:193], v[130:133]
	v_mfma_f32_16x16x32_bf16 v[126:129], v[158:161], v[190:193], v[126:129]
	v_mfma_f32_16x16x32_bf16 v[122:125], v[150:153], v[198:201], v[122:125]
	v_mfma_f32_16x16x32_bf16 v[118:121], v[158:161], v[198:201], v[118:121]
	v_mfma_f32_16x16x32_bf16 v[114:117], v[150:153], v[228:231], v[114:117]
	v_mfma_f32_16x16x32_bf16 v[106:109], v[158:161], v[228:231], v[106:109]
	v_mfma_f32_16x16x32_bf16 v[98:101], v[150:153], v[236:239], v[98:101]
	v_mfma_f32_16x16x32_bf16 v[90:93], v[158:161], v[236:239], v[90:93]
	s_setprio 0
	s_setprio 1
	v_mfma_f32_16x16x32_bf16 v[110:113], v[166:169], v[186:189], v[110:113]
	v_mfma_f32_16x16x32_bf16 v[102:105], v[174:177], v[186:189], v[102:105]
	v_mfma_f32_16x16x32_bf16 v[94:97], v[166:169], v[194:197], v[94:97]
	v_mfma_f32_16x16x32_bf16 v[86:89], v[174:177], v[194:197], v[86:89]
	v_mfma_f32_16x16x32_bf16 v[82:85], v[166:169], v[224:227], v[82:85]
	v_mfma_f32_16x16x32_bf16 v[78:81], v[174:177], v[224:227], v[78:81]
	v_mfma_f32_16x16x32_bf16 v[74:77], v[166:169], v[232:235], v[74:77]
	v_mfma_f32_16x16x32_bf16 v[70:73], v[174:177], v[232:235], v[70:73]
	v_mfma_f32_16x16x32_bf16 v[110:113], v[170:173], v[190:193], v[110:113]
	v_mfma_f32_16x16x32_bf16 v[102:105], v[178:181], v[190:193], v[102:105]
	v_mfma_f32_16x16x32_bf16 v[94:97], v[170:173], v[198:201], v[94:97]
	v_mfma_f32_16x16x32_bf16 v[86:89], v[178:181], v[198:201], v[86:89]
	v_mfma_f32_16x16x32_bf16 v[82:85], v[170:173], v[228:231], v[82:85]
	v_mfma_f32_16x16x32_bf16 v[78:81], v[178:181], v[228:231], v[78:81]
	v_mfma_f32_16x16x32_bf16 v[74:77], v[170:173], v[236:239], v[74:77]
	v_mfma_f32_16x16x32_bf16 v[70:73], v[178:181], v[236:239], v[70:73]
	s_setprio 0
	s_barrier
	s_add_i32 s22, s33, s34
	v_lshl_add_u64 v[182:183], v[182:183], 0, s[46:47]
	s_mov_b32 m0, s22
	ds_read_b128 v[186:189], v164 offset:49152
	ds_read_b128 v[190:193], v164 offset:50176
	ds_read_b128 v[194:197], v164 offset:51200
	ds_read_b128 v[198:201], v164 offset:52224
	ds_read_b128 v[224:227], v164 offset:53248
	ds_read_b128 v[228:231], v164 offset:54272
	ds_read_b128 v[232:235], v164 offset:55296
	ds_read_b128 v[236:239], v164 offset:56320
	global_load_lds_dwordx4 v[182:183], off
	s_add_i32 m0, s22, 0x2000
	s_add_u32 s20, s20, 0x40080
	v_lshl_add_u64 v[182:183], v[184:185], 0, s[46:47]
	s_addc_u32 s21, s21, 0
	s_add_i32 s22, s40, s34
	global_load_lds_dwordx4 v[182:183], off
	v_lshl_add_u64 v[182:183], s[20:21], 0, v[0:1]
	s_mov_b32 m0, s22
	s_nop 0
	global_load_lds_dwordx4 v[182:183], off
	v_lshl_add_u64 v[182:183], s[20:21], 0, v[138:139]
	s_add_i32 m0, s22, 0x2000
	s_nop 0
	global_load_lds_dwordx4 v[182:183], off
	v_lshl_add_u64 v[182:183], v[202:203], 0, s[46:47]
	s_mov_b32 m0, s38
	s_nop 0
	global_load_lds_dwordx4 v[182:183], off
	v_lshl_add_u64 v[182:183], v[210:211], 0, s[46:47]
	s_mov_b32 m0, s39
	s_nop 0
	global_load_lds_dwordx4 v[182:183], off
	s_waitcnt vmcnt(8)
	s_waitcnt lgkmcnt(0)
	s_barrier
	s_setprio 1
	s_waitcnt lgkmcnt(0)
	v_mfma_f32_16x16x32_bf16 v[66:69], v[146:149], v[186:189], v[66:69]
	v_mfma_f32_16x16x32_bf16 v[62:65], v[154:157], v[186:189], v[62:65]
	v_mfma_f32_16x16x32_bf16 v[58:61], v[146:149], v[194:197], v[58:61]
	v_mfma_f32_16x16x32_bf16 v[54:57], v[154:157], v[194:197], v[54:57]
	v_mfma_f32_16x16x32_bf16 v[50:53], v[146:149], v[224:227], v[50:53]
	v_mfma_f32_16x16x32_bf16 v[42:45], v[154:157], v[224:227], v[42:45]
	v_mfma_f32_16x16x32_bf16 v[30:33], v[146:149], v[232:235], v[30:33]
	v_mfma_f32_16x16x32_bf16 v[22:25], v[154:157], v[232:235], v[22:25]
	v_mfma_f32_16x16x32_bf16 v[66:69], v[150:153], v[190:193], v[66:69]
	v_mfma_f32_16x16x32_bf16 v[62:65], v[158:161], v[190:193], v[62:65]
	v_mfma_f32_16x16x32_bf16 v[58:61], v[150:153], v[198:201], v[58:61]
	v_mfma_f32_16x16x32_bf16 v[54:57], v[158:161], v[198:201], v[54:57]
	v_mfma_f32_16x16x32_bf16 v[50:53], v[150:153], v[228:231], v[50:53]
	v_mfma_f32_16x16x32_bf16 v[42:45], v[158:161], v[228:231], v[42:45]
	v_mfma_f32_16x16x32_bf16 v[30:33], v[150:153], v[236:239], v[30:33]
	v_mfma_f32_16x16x32_bf16 v[22:25], v[158:161], v[236:239], v[22:25]
	s_setprio 0
	s_setprio 1
	v_mfma_f32_16x16x32_bf16 v[46:49], v[166:169], v[186:189], v[46:49]
	v_mfma_f32_16x16x32_bf16 v[38:41], v[174:177], v[186:189], v[38:41]
	v_mfma_f32_16x16x32_bf16 v[26:29], v[166:169], v[194:197], v[26:29]
	v_mfma_f32_16x16x32_bf16 v[18:21], v[174:177], v[194:197], v[18:21]
	v_mfma_f32_16x16x32_bf16 v[14:17], v[166:169], v[224:227], v[14:17]
	v_mfma_f32_16x16x32_bf16 v[10:13], v[174:177], v[224:227], v[10:13]
	v_mfma_f32_16x16x32_bf16 v[6:9], v[166:169], v[232:235], v[6:9]
	v_mfma_f32_16x16x32_bf16 v[2:5], v[174:177], v[232:235], v[2:5]
	v_mfma_f32_16x16x32_bf16 v[46:49], v[170:173], v[190:193], v[46:49]
	v_mfma_f32_16x16x32_bf16 v[38:41], v[178:181], v[190:193], v[38:41]
	v_mfma_f32_16x16x32_bf16 v[26:29], v[170:173], v[198:201], v[26:29]
	v_mfma_f32_16x16x32_bf16 v[18:21], v[178:181], v[198:201], v[18:21]
	v_mfma_f32_16x16x32_bf16 v[14:17], v[170:173], v[228:231], v[14:17]
	v_mfma_f32_16x16x32_bf16 v[10:13], v[178:181], v[228:231], v[10:13]
	v_mfma_f32_16x16x32_bf16 v[6:9], v[170:173], v[236:239], v[6:9]
	v_mfma_f32_16x16x32_bf16 v[2:5], v[178:181], v[236:239], v[2:5]
	s_setprio 0
	s_barrier
	s_add_i32 s55, s55, 2
	s_add_u32 s53, s53, 0x100
	s_addc_u32 s54, s54, 0
	s_add_u32 s18, s18, 0x100
	s_addc_u32 s19, s19, 0
